# P0 weight-panel loop rewritten by hand: 256B-wide double panels (two adjacent 32-col panels loaded together, dwordx4 nt loads), lean max/convert, mode-3 panels via compiler path on lighter WGs
# speedup vs baseline: 1.0197x; 1.0118x over previous
; #define LAS __attribute__((address_space(3)))
; __device__ __forceinline__ const GAS float* inp(const Frame& F, int i) { return (const GAS float*)*(const float* const __attribute__((address_space(4)))*)(F.ka + 8 * i); }
; __device__ __forceinline__ bf16* w_in_t(Frame& F, int l)  { return (bf16*)(F.ws + WS_W + (size_t)l * W_LAYER_B); }
; __device__ __forceinline__ PanelSrc p0_panel_src(Frame& F, int it) {
;     constexpr int P_IN = (NPROJ + 31) / 32 + 8, P_GU = 2048 / 32, P_DN = D / 32, PAN_LAYER = P_IN + NEXP * P_GU + NEXP * P_DN;
;     const int l = it / PAN_LAYER; int r = it % PAN_LAYER; PanelSrc s; s.W2 = inp(F, 4) + (size_t)l * GLR_RANK * 256;
;     if (r < P_IN) { s.W = inp(F, 3) + (size_t)l * D * NPROJ; s.N = NPROJ; s.WT = (signed char*)w_in_t(F, l); s.cmax = F.ctl + CW_CMAX_IN + l * NPROJ_PAD; s.fp8 = 0;
;         if (r < P_IN - 8) { s.p = r; s.mode = 2; } else { s.p = r - (P_IN - 8); s.mode = 3; } }
;     else if (r < P_IN + NEXP * P_GU) { r -= P_IN; const int e = r / P_GU; s.W = inp(F, 15) + ((size_t)l * NEXP + e) * D * 2048; s.N = 2048; s.WT = (signed char*)w_gu_t(F, l) + (size_t)e * 2048 * D; s.cmax = F.ctl + CW_CMAX_GU + (l * NEXP + e) * 2048; s.p = r % P_GU; s.mode = 1; s.fp8 = 0; }
;     else { r -= P_IN + NEXP * P_GU; const int e = r / P_DN; s.W = inp(F, 17) + ((size_t)l * NEXP + e) * DFF * D; s.N = D; s.WT = (signed char*)w_dn_t(F, l) + (size_t)e * D * DFF; s.cmax = F.ctl + CW_CMAX_DN + (l * NEXP + e) * D; s.p = r % P_DN; s.mode = 0; s.fp8 = 1; }
;     return s;
; __device__ __forceinline__ void p0_panels(Frame& F) {
;     constexpr int P_IN = (NPROJ + 31) / 32 + 8, P_GU = 2048 / 32, P_DN = D / 32, PAN_LAYER = P_IN + NEXP * P_GU + NEXP * P_DN, NPAN = DEPTH * PAN_LAYER;
;     LAS float* pan = (LAS float*)F.lds; LAS float* pmx = (LAS float*)(F.lds + TOK_OFF);
;     const int tid = F.tid, lane = F.lane, wave = F.wave;
;     int it = F.vcu; if (it >= NPAN) return;
;     float rg[64]; PanelSrc cur = p0_panel_src(F, it); p0_panel_load(F, cur, rg);
;     for (;;) {
; #pragma unroll
;         for (int i = 0; i < 64; ++i) { const int k = 2 * (8 * i + wave) + (lane >> 5); pan[k * 32 + (lane & 31)] = rg[i]; }
;         lds_barrier();
;         const int itn = it + F.G; const bool more = itn < NPAN; PanelSrc nxt = cur; if (more) { nxt = p0_panel_src(F, itn); p0_panel_load(F, nxt, rg); }
.LBB0_6:
	s_or_b64 exec, exec, s[4:5]
	v_mov_b32_e32 v0, s1
	v_mov_b32_e32 v3, s0
	s_lshr_b32 s92, s30, 6
	v_readfirstlane_b32 s40, v3
	v_readfirstlane_b32 s41, v0
	v_mov_b32_e32 v0, s39
	v_mov_b32_e32 v3, s38
	s_lshl_b32 s1, s92, 1
	v_writelane_b32 v252, s1, 2
	s_lshl_b32 s1, s92, 8
	v_readfirstlane_b32 s43, v0
	v_mbcnt_lo_u32_b32 v0, -1, 0
	s_and_b32 s31, s30, 0xffffffc0
	v_writelane_b32 v252, s1, 3
	v_mbcnt_hi_u32_b32 v59, -1, v0
	v_or_b32_e32 v179, s31, v59
	v_writelane_b32 v252, s90, 4
	s_mov_b32 s0, s8
	v_mov_b32_e32 v1, s36
	v_mov_b32_e32 v2, s37
	v_mov_b32_e32 v61, v179
	v_writelane_b32 v252, s0, 5
	s_cmpk_gt_i32 s8, 0x18e1
	v_readfirstlane_b32 s42, v3
	v_writelane_b32 v252, s1, 6
	v_readfirstlane_b32 s44, v1
	v_readfirstlane_b32 s45, v2
	v_and_b32_e32 v113, 63, v61
	s_cbranch_scc1 .LBB0_255
	s_mov_b32 s99, 0
	s_cmpk_lg_u32 s94, 0x100
	s_cbranch_scc1 .Lp0h_orig
	s_load_dwordx2 s[50:51], s[40:41], 0x18
	s_load_dwordx2 s[52:53], s[40:41], 0x78
	s_load_dwordx2 s[54:55], s[40:41], 0x88
	v_lshrrev_b32_e32 v72, 3, v179
	v_and_b32_e32 v73, 7, v179
	v_lshlrev_b32_e32 v73, 4, v73
	v_lshlrev_b32_e32 v74, 4, v179
	v_add_u32_e32 v75, 0x10000, v74
	v_and_b32_e32 v76, 31, v179
	v_lshrrev_b32_e32 v77, 5, v179
	v_lshlrev_b32_e32 v78, 13, v77
	v_lshl_or_b32 v78, v76, 2, v78
	v_lshlrev_b32_e32 v79, 2, v179
	v_add_u32_e32 v79, 0x20900, v79
	v_lshlrev_b32_e32 v80, 2, v76
	v_add_u32_e32 v81, 0x20900, v80
	v_add_u32_e32 v82, 0x400, v81
	v_lshlrev_b32_e32 v83, 10, v76
	v_lshl_or_b32 v83, v77, 6, v83
	v_cmp_gt_u32_e32 vcc, 32, v179
	s_mov_b64 s[56:57], vcc
	s_mov_b32 s86, 0x4b400000
	s_mov_b32 s87, 0x4b400000
	s_mov_b32 s88, 0x0c0c0400
	s_mov_b32 s89, 0x04000c0c
	s_mov_b32 s84, s8
	s_cmpk_lt_i32 s84, 0x635
	s_cselect_b32 s65, 0, 0x635
	s_cselect_b32 s66, 0, 0xc71
	s_sub_i32 s67, s84, s65
	s_mov_b32 s83, 1
	s_cmpk_lt_i32 s67, 53
	s_cbranch_scc0 .Lp0h_cv_gu_c0
	s_lshl_b32 s68, s67, 1
	s_cmpk_eq_i32 s67, 52
	s_cselect_b32 s83, 0, 1
	s_branch .Lp0h_cv_done_c0
.Lp0h_cv_gu_c0:
	s_cmpk_lt_i32 s67, 0x435
	s_cbranch_scc0 .Lp0h_cv_dn_c0
	s_lshl_b32 s68, s67, 1
	s_add_i32 s68, s68, 7
	s_branch .Lp0h_cv_done_c0
.Lp0h_cv_dn_c0:
	s_lshl_b32 s68, s67, 1
	s_add_i32 s68, s68, 7
.Lp0h_cv_done_c0:
	s_add_i32 s80, s68, s66
	s_waitcnt lgkmcnt(0)
	s_cmpk_lt_i32 s80, 0xc71
	s_cselect_b32 s65, 0, 0xc71
	s_cselect_b32 s66, 0, 1
	s_sub_i32 s67, s80, s65
	s_mov_b32 s64, 0
	s_cmpk_lt_i32 s67, 0x71
	s_cbranch_scc0 .Lp0h_dl_gu_p0
	s_mul_i32 s68, s66, 0xd10000
	s_lshl_b32 s69, s67, 7
	s_add_u32 s68, s68, s69
	s_add_u32 s60, s50, s68
	s_addc_u32 s61, s51, 0
	s_movk_i32 s62, 0x3440
	s_mov_b32 s63, 0xd1000
	s_cmpk_eq_i32 s67, 0x68
	s_cselect_b32 s64, 1, 0
	s_branch .Lp0h_dl_done_p0
.Lp0h_dl_gu_p0:
	s_cmpk_lt_i32 s67, 0x871
	s_cbranch_scc0 .Lp0h_dl_dn_p0
	s_sub_i32 s67, s67, 0x71
	s_lshr_b32 s68, s67, 6
	s_and_b32 s69, s67, 63
	s_lshl_b32 s70, s66, 5
	s_add_i32 s68, s68, s70
	s_lshl_b32 s68, s68, 23
	s_lshl_b32 s69, s69, 7
	s_add_u32 s68, s68, s69
	s_add_u32 s60, s52, s68
	s_addc_u32 s61, s53, 0
	s_movk_i32 s62, 0x2000
	s_mov_b32 s63, 0x80000
	s_branch .Lp0h_dl_done_p0
.Lp0h_dl_dn_p0:
	s_sub_i32 s67, s67, 0x871
	s_lshr_b32 s68, s67, 5
	s_and_b32 s69, s67, 31
	s_lshl_b32 s70, s66, 5
	s_add_i32 s68, s68, s70
	s_lshl_b32 s68, s68, 22
	s_lshl_b32 s69, s69, 7
	s_add_u32 s68, s68, s69
	s_add_u32 s60, s54, s68
	s_addc_u32 s61, s55, 0
	s_movk_i32 s62, 0x1000
	s_mov_b32 s63, 0x40000
.Lp0h_dl_done_p0:
	v_mad_u32_u24 v87, v72, s62, v73
	s_cmp_eq_u32 s64, 0
	s_cbranch_scc1 .Lp0h_full_p0
	v_mov_b32_e32 v180, 0
	v_mov_b32_e32 v181, 0
	v_mov_b32_e32 v182, 0
	v_mov_b32_e32 v183, 0
	v_mov_b32_e32 v184, 0
	v_mov_b32_e32 v185, 0
	v_mov_b32_e32 v186, 0
	v_mov_b32_e32 v187, 0
	v_mov_b32_e32 v188, 0
	v_mov_b32_e32 v189, 0
	v_mov_b32_e32 v190, 0
	v_mov_b32_e32 v191, 0
	v_mov_b32_e32 v192, 0
	v_mov_b32_e32 v193, 0
	v_mov_b32_e32 v194, 0
	v_mov_b32_e32 v195, 0
	v_mov_b32_e32 v196, 0
	v_mov_b32_e32 v197, 0
	v_mov_b32_e32 v198, 0
	v_mov_b32_e32 v199, 0
	v_mov_b32_e32 v200, 0
	v_mov_b32_e32 v201, 0
	v_mov_b32_e32 v202, 0
	v_mov_b32_e32 v203, 0
	v_mov_b32_e32 v204, 0
	v_mov_b32_e32 v205, 0
	v_mov_b32_e32 v206, 0
	v_mov_b32_e32 v207, 0
	v_mov_b32_e32 v208, 0
	v_mov_b32_e32 v209, 0
	v_mov_b32_e32 v210, 0
	v_mov_b32_e32 v211, 0
	v_mov_b32_e32 v212, 0
	v_mov_b32_e32 v213, 0
	v_mov_b32_e32 v214, 0
	v_mov_b32_e32 v215, 0
	v_mov_b32_e32 v216, 0
	v_mov_b32_e32 v217, 0
	v_mov_b32_e32 v218, 0
	v_mov_b32_e32 v219, 0
	v_mov_b32_e32 v220, 0
	v_mov_b32_e32 v221, 0
	v_mov_b32_e32 v222, 0
	v_mov_b32_e32 v223, 0
	v_mov_b32_e32 v224, 0
	v_mov_b32_e32 v225, 0
	v_mov_b32_e32 v226, 0
	v_mov_b32_e32 v227, 0
	v_mov_b32_e32 v228, 0
	v_mov_b32_e32 v229, 0
	v_mov_b32_e32 v230, 0
	v_mov_b32_e32 v231, 0
	v_mov_b32_e32 v232, 0
	v_mov_b32_e32 v233, 0
	v_mov_b32_e32 v234, 0
	v_mov_b32_e32 v235, 0
	v_mov_b32_e32 v236, 0
	v_mov_b32_e32 v237, 0
	v_mov_b32_e32 v238, 0
	v_mov_b32_e32 v239, 0
	v_mov_b32_e32 v240, 0
	v_mov_b32_e32 v241, 0
	v_mov_b32_e32 v242, 0
	v_mov_b32_e32 v243, 0
	s_mov_b32 s68, 0x0f0f0f0f
	s_mov_b32 s69, 0x0f0f0f0f
	s_mov_b64 exec, s[68:69]
	global_load_dwordx4 v[180:183], v87, s[60:61] nt
	s_add_u32 s60, s60, s63
	s_addc_u32 s61, s61, 0
	global_load_dwordx4 v[184:187], v87, s[60:61] nt
	s_add_u32 s60, s60, s63
	s_addc_u32 s61, s61, 0
	global_load_dwordx4 v[188:191], v87, s[60:61] nt
	s_add_u32 s60, s60, s63
	s_addc_u32 s61, s61, 0
	global_load_dwordx4 v[192:195], v87, s[60:61] nt
	s_add_u32 s60, s60, s63
	s_addc_u32 s61, s61, 0
	global_load_dwordx4 v[196:199], v87, s[60:61] nt
	s_add_u32 s60, s60, s63
	s_addc_u32 s61, s61, 0
	global_load_dwordx4 v[200:203], v87, s[60:61] nt
	s_add_u32 s60, s60, s63
	s_addc_u32 s61, s61, 0
	global_load_dwordx4 v[204:207], v87, s[60:61] nt
	s_add_u32 s60, s60, s63
	s_addc_u32 s61, s61, 0
	global_load_dwordx4 v[208:211], v87, s[60:61] nt
	s_add_u32 s60, s60, s63
	s_addc_u32 s61, s61, 0
	global_load_dwordx4 v[212:215], v87, s[60:61] nt
	s_add_u32 s60, s60, s63
	s_addc_u32 s61, s61, 0
	global_load_dwordx4 v[216:219], v87, s[60:61] nt
	s_add_u32 s60, s60, s63
	s_addc_u32 s61, s61, 0
	global_load_dwordx4 v[220:223], v87, s[60:61] nt
	s_add_u32 s60, s60, s63
	s_addc_u32 s61, s61, 0
	global_load_dwordx4 v[224:227], v87, s[60:61] nt
	s_add_u32 s60, s60, s63
	s_addc_u32 s61, s61, 0
	global_load_dwordx4 v[228:231], v87, s[60:61] nt
	s_add_u32 s60, s60, s63
	s_addc_u32 s61, s61, 0
	global_load_dwordx4 v[232:235], v87, s[60:61] nt
	s_add_u32 s60, s60, s63
	s_addc_u32 s61, s61, 0
	global_load_dwordx4 v[236:239], v87, s[60:61] nt
	s_add_u32 s60, s60, s63
	s_addc_u32 s61, s61, 0
	global_load_dwordx4 v[240:243], v87, s[60:61] nt
	s_mov_b64 exec, -1
	s_branch .Lp0h_ldone_p0
; __device__ __forceinline__ void lds_barrier() { asm volatile("s_waitcnt lgkmcnt(0)" ::: "memory"); __builtin_amdgcn_s_barrier(); asm volatile("" ::: "memory"); }
; __device__ __forceinline__ void p0_panels(Frame& F) {
;     ...
;         for (int i = 0; i < 64; ++i) { const int k = 2 * (8 * i + wave) + (lane >> 5); pan[k * 32 + (lane & 31)] = rg[i]; }
;         lds_barrier();
;     ...
;         const int ns = 32 * cur.p + n; int nd = ns; bool okc = ns < cur.N;
;         if (cur.mode == 1) { const int half = ns >> 10, cc = ns & 1023; nd = (cc >> 7) * 256 + half * 128 + (cc & 127); }
;         else if (cur.mode == 2) { nd = ns < SRC_GLR ? ns : ns + (C_GOG - SRC_GLR - GLR_RANK); okc = okc && !(ns >= SRC_GLR && ns < SRC_GLR + GLR_RANK); }
;         else if (cur.mode == 3) { nd = C_GLG + ns; okc = ns < 256; }
;         if (okc) {
;             if (ks == 0) cur.cmax[nd] = __float_as_uint(cm);
.Lp0h_full_p0:
	global_load_dwordx4 v[180:183], v87, s[60:61] nt
	global_load_dwordx4 v[114:117], v87, s[60:61] offset:128 nt
	s_add_u32 s60, s60, s63
	s_addc_u32 s61, s61, 0
	global_load_dwordx4 v[184:187], v87, s[60:61] nt
	global_load_dwordx4 v[118:121], v87, s[60:61] offset:128 nt
	s_add_u32 s60, s60, s63
	s_addc_u32 s61, s61, 0
	global_load_dwordx4 v[188:191], v87, s[60:61] nt
	global_load_dwordx4 v[122:125], v87, s[60:61] offset:128 nt
	s_add_u32 s60, s60, s63
	s_addc_u32 s61, s61, 0
	global_load_dwordx4 v[192:195], v87, s[60:61] nt
	global_load_dwordx4 v[126:129], v87, s[60:61] offset:128 nt
	s_add_u32 s60, s60, s63
	s_addc_u32 s61, s61, 0
	global_load_dwordx4 v[196:199], v87, s[60:61] nt
	global_load_dwordx4 v[130:133], v87, s[60:61] offset:128 nt
	s_add_u32 s60, s60, s63
	s_addc_u32 s61, s61, 0
	global_load_dwordx4 v[200:203], v87, s[60:61] nt
	global_load_dwordx4 v[134:137], v87, s[60:61] offset:128 nt
	s_add_u32 s60, s60, s63
	s_addc_u32 s61, s61, 0
	global_load_dwordx4 v[204:207], v87, s[60:61] nt
	global_load_dwordx4 v[138:141], v87, s[60:61] offset:128 nt
	s_add_u32 s60, s60, s63
	s_addc_u32 s61, s61, 0
	global_load_dwordx4 v[208:211], v87, s[60:61] nt
	global_load_dwordx4 v[142:145], v87, s[60:61] offset:128 nt
	s_add_u32 s60, s60, s63
	s_addc_u32 s61, s61, 0
	global_load_dwordx4 v[212:215], v87, s[60:61] nt
	global_load_dwordx4 v[146:149], v87, s[60:61] offset:128 nt
	s_add_u32 s60, s60, s63
	s_addc_u32 s61, s61, 0
	global_load_dwordx4 v[216:219], v87, s[60:61] nt
	global_load_dwordx4 v[150:153], v87, s[60:61] offset:128 nt
	s_add_u32 s60, s60, s63
	s_addc_u32 s61, s61, 0
	global_load_dwordx4 v[220:223], v87, s[60:61] nt
	global_load_dwordx4 v[154:157], v87, s[60:61] offset:128 nt
	s_add_u32 s60, s60, s63
	s_addc_u32 s61, s61, 0
	global_load_dwordx4 v[224:227], v87, s[60:61] nt
	global_load_dwordx4 v[158:161], v87, s[60:61] offset:128 nt
	s_add_u32 s60, s60, s63
	s_addc_u32 s61, s61, 0
	global_load_dwordx4 v[228:231], v87, s[60:61] nt
	global_load_dwordx4 v[162:165], v87, s[60:61] offset:128 nt
	s_add_u32 s60, s60, s63
	s_addc_u32 s61, s61, 0
	global_load_dwordx4 v[232:235], v87, s[60:61] nt
	global_load_dwordx4 v[166:169], v87, s[60:61] offset:128 nt
	s_add_u32 s60, s60, s63
	s_addc_u32 s61, s61, 0
	global_load_dwordx4 v[236:239], v87, s[60:61] nt
	global_load_dwordx4 v[170:173], v87, s[60:61] offset:128 nt
	s_add_u32 s60, s60, s63
	s_addc_u32 s61, s61, 0
	global_load_dwordx4 v[240:243], v87, s[60:61] nt
	global_load_dwordx4 v[174:177], v87, s[60:61] offset:128 nt
.Lp0h_ldone_p0:
.Lp0h_top:
	s_waitcnt vmcnt(0)
	ds_write_b128 v74, v[180:183]
	ds_write_b128 v74, v[184:187] offset:8192
	ds_write_b128 v74, v[188:191] offset:16384
	ds_write_b128 v74, v[192:195] offset:24576
	ds_write_b128 v74, v[196:199] offset:32768
	ds_write_b128 v74, v[200:203] offset:40960
	ds_write_b128 v74, v[204:207] offset:49152
	ds_write_b128 v74, v[208:211] offset:57344
	ds_write_b128 v75, v[212:215]
	ds_write_b128 v75, v[216:219] offset:8192
	ds_write_b128 v75, v[220:223] offset:16384
	ds_write_b128 v75, v[224:227] offset:24576
	ds_write_b128 v75, v[228:231] offset:32768
	ds_write_b128 v75, v[232:235] offset:40960
	ds_write_b128 v75, v[236:239] offset:49152
	ds_write_b128 v75, v[240:243] offset:57344
	s_waitcnt lgkmcnt(0)
	s_barrier
	s_cmpk_lt_i32 s80, 0xc71
	s_cselect_b32 s65, 0, 0xc71
	s_cselect_b32 s66, 0, 1
	s_sub_i32 s67, s80, s65
	s_mul_i32 s70, s66, 0xc900000
	s_mov_b64 s[76:77], -1
	s_mov_b32 s79, 0x42fe0000
	s_cmpk_lt_i32 s67, 0x71
	s_cbranch_scc0 .Lp0h_dp_gu_A
	s_lshl_b32 s71, s67, 5
	s_cmpk_lt_i32 s67, 32
	s_cselect_b32 s68, 0, 0xf0
	s_add_i32 s71, s71, s68
	s_add_u32 s70, s70, 0x200000
	s_mul_i32 s69, s66, 0x3800
	s_add_u32 s69, s69, 0x40000
	s_mov_b32 s78, 0
	s_cmpk_eq_i32 s67, 32
	s_cbranch_scc0 .Lp0h_dp_m2a_A
	s_mov_b32 s76, 0xffff0000
	s_mov_b32 s77, 0xffff0000
.Lp0h_dp_m2a_A:
	s_cmpk_eq_i32 s67, 0x68
	s_cbranch_scc0 .Lp0h_dp_done_A
	s_mov_b32 s76, 0x0000ffff
	s_mov_b32 s77, 0x0000ffff
	s_branch .Lp0h_dp_done_A
.Lp0h_dp_gu_A:
	s_cmpk_lt_i32 s67, 0x871
	s_cbranch_scc0 .Lp0h_dp_dn_A
	s_sub_i32 s67, s67, 0x71
	s_lshr_b32 s68, s67, 6
	s_and_b32 s67, s67, 63
	s_lshl_b32 s69, s68, 21
	s_add_u32 s70, s70, s69
	s_add_u32 s70, s70, 0xb00000
	s_lshl_b32 s69, s66, 5
	s_add_i32 s69, s69, s68
	s_lshl_b32 s69, s69, 13
	s_add_u32 s69, s69, 0x48000
	s_bfe_u32 s71, s67, 0x30002
	s_lshl_b32 s71, s71, 8
	s_lshr_b32 s68, s67, 5
	s_lshl_b32 s68, s68, 7
	s_add_i32 s71, s71, s68
	s_and_b32 s68, s67, 3
	s_lshl_b32 s68, s68, 5
	s_add_i32 s71, s71, s68
	s_mov_b32 s78, 0
	s_branch .Lp0h_dp_done_A
.Lp0h_dp_dn_A:
	s_sub_i32 s67, s67, 0x871
	s_lshr_b32 s68, s67, 5
	s_and_b32 s67, s67, 31
	s_lshl_b32 s69, s68, 20
	s_add_u32 s70, s70, s69
	s_add_u32 s70, s70, 0x8b00000
	s_lshl_b32 s69, s66, 5
	s_add_i32 s69, s69, s68
	s_lshl_b32 s69, s69, 12
	s_add_u32 s69, s69, 0x100000
	s_lshl_b32 s71, s67, 5
	s_mov_b32 s78, 1
	s_mov_b32 s79, 0x43df8000
; __device__ __forceinline__ void lds_barrier() { asm volatile("s_waitcnt lgkmcnt(0)" ::: "memory"); __builtin_amdgcn_s_barrier(); asm volatile("" ::: "memory"); }
; __device__ __forceinline__ void p0_panels(Frame& F) {
;     ...
;         const int itn = it + F.G; const bool more = itn < NPAN; PanelSrc nxt = cur; if (more) { nxt = p0_panel_src(F, itn); p0_panel_load(F, nxt, rg); }
;         const int n = tid & 31, ks = tid >> 5;
;         float mx = 0.f;
; #pragma unroll 8
;         for (int i = 0; i < 64; ++i) mx = fmaxf(mx, fabsf(pan[(64 * ks + i) * 32 + n]));
;         pmx[ks * 32 + n] = mx;
;         lds_barrier();
;         float cm = 0.f;
; #pragma unroll
;         for (int q = 0; q < 16; ++q) cm = fmaxf(cm, pmx[q * 32 + n]);
;         const float inv = cm > 0.f ? (cur.fp8 ? pg8::WDN_SC : 127.0f) / cm : 0.f;
.Lp0h_dp_done_A:
	s_lshl_b32 s68, s71, 10
	s_add_u32 s70, s70, s68
	s_add_u32 s72, s42, s70
	s_addc_u32 s73, s43, 0
	s_lshl_b32 s68, s71, 2
	s_add_u32 s69, s69, s68
	s_add_u32 s74, s42, s69
	s_addc_u32 s75, s43, 0
	ds_read_b32 v4, v78
	ds_read_b32 v5, v78 offset:128
	ds_read_b32 v6, v78 offset:256
	ds_read_b32 v7, v78 offset:384
	ds_read_b32 v8, v78 offset:512
	ds_read_b32 v9, v78 offset:640
	ds_read_b32 v10, v78 offset:768
	ds_read_b32 v11, v78 offset:896
	ds_read_b32 v12, v78 offset:1024
	ds_read_b32 v13, v78 offset:1152
	ds_read_b32 v14, v78 offset:1280
	ds_read_b32 v15, v78 offset:1408
	ds_read_b32 v16, v78 offset:1536
	ds_read_b32 v17, v78 offset:1664
	ds_read_b32 v18, v78 offset:1792
	ds_read_b32 v19, v78 offset:1920
	ds_read_b32 v20, v78 offset:2048
	ds_read_b32 v21, v78 offset:2176
	ds_read_b32 v22, v78 offset:2304
	ds_read_b32 v23, v78 offset:2432
	ds_read_b32 v24, v78 offset:2560
	ds_read_b32 v25, v78 offset:2688
	ds_read_b32 v26, v78 offset:2816
	ds_read_b32 v27, v78 offset:2944
	ds_read_b32 v28, v78 offset:3072
	ds_read_b32 v29, v78 offset:3200
	ds_read_b32 v30, v78 offset:3328
	ds_read_b32 v31, v78 offset:3456
	ds_read_b32 v32, v78 offset:3584
	ds_read_b32 v33, v78 offset:3712
	ds_read_b32 v34, v78 offset:3840
	ds_read_b32 v35, v78 offset:3968
	ds_read_b32 v36, v78 offset:4096
	ds_read_b32 v37, v78 offset:4224
	ds_read_b32 v38, v78 offset:4352
	ds_read_b32 v39, v78 offset:4480
	ds_read_b32 v40, v78 offset:4608
	ds_read_b32 v41, v78 offset:4736
	ds_read_b32 v42, v78 offset:4864
	ds_read_b32 v43, v78 offset:4992
	ds_read_b32 v44, v78 offset:5120
	ds_read_b32 v45, v78 offset:5248
	ds_read_b32 v46, v78 offset:5376
	ds_read_b32 v47, v78 offset:5504
	ds_read_b32 v48, v78 offset:5632
	ds_read_b32 v49, v78 offset:5760
	ds_read_b32 v50, v78 offset:5888
	ds_read_b32 v51, v78 offset:6016
	ds_read_b32 v52, v78 offset:6144
	ds_read_b32 v53, v78 offset:6272
	ds_read_b32 v54, v78 offset:6400
	ds_read_b32 v55, v78 offset:6528
	ds_read_b32 v56, v78 offset:6656
	ds_read_b32 v57, v78 offset:6784
	ds_read_b32 v62, v78 offset:6912
	ds_read_b32 v63, v78 offset:7040
	ds_read_b32 v64, v78 offset:7168
	ds_read_b32 v65, v78 offset:7296
	ds_read_b32 v66, v78 offset:7424
	ds_read_b32 v67, v78 offset:7552
	ds_read_b32 v68, v78 offset:7680
	ds_read_b32 v69, v78 offset:7808
	ds_read_b32 v70, v78 offset:7936
	ds_read_b32 v71, v78 offset:8064
	s_waitcnt lgkmcnt(0)
	v_max_f32_e64 v104, |v4|, |v5|
	v_max3_f32 v104, v104, |v6|, |v7|
	v_max3_f32 v104, v104, |v8|, |v9|
	v_max3_f32 v104, v104, |v10|, |v11|
	v_max3_f32 v104, v104, |v12|, |v13|
	v_max3_f32 v104, v104, |v14|, |v15|
	v_max3_f32 v104, v104, |v16|, |v17|
	v_max3_f32 v104, v104, |v18|, |v19|
	v_max3_f32 v104, v104, |v20|, |v21|
	v_max3_f32 v104, v104, |v22|, |v23|
	v_max3_f32 v104, v104, |v24|, |v25|
	v_max3_f32 v104, v104, |v26|, |v27|
	v_max3_f32 v104, v104, |v28|, |v29|
	v_max3_f32 v104, v104, |v30|, |v31|
	v_max3_f32 v104, v104, |v32|, |v33|
	v_max3_f32 v104, v104, |v34|, |v35|
	v_max3_f32 v104, v104, |v36|, |v37|
	v_max3_f32 v104, v104, |v38|, |v39|
	v_max3_f32 v104, v104, |v40|, |v41|
	v_max3_f32 v104, v104, |v42|, |v43|
	v_max3_f32 v104, v104, |v44|, |v45|
	v_max3_f32 v104, v104, |v46|, |v47|
	v_max3_f32 v104, v104, |v48|, |v49|
	v_max3_f32 v104, v104, |v50|, |v51|
	v_max3_f32 v104, v104, |v52|, |v53|
	v_max3_f32 v104, v104, |v54|, |v55|
	v_max3_f32 v104, v104, |v56|, |v57|
	v_max3_f32 v104, v104, |v62|, |v63|
	v_max3_f32 v104, v104, |v64|, |v65|
	v_max3_f32 v104, v104, |v66|, |v67|
	v_max3_f32 v104, v104, |v68|, |v69|
	v_max3_f32 v104, v104, |v70|, |v71|
	ds_write_b32 v79, v104
	s_waitcnt lgkmcnt(0)
	s_barrier
	ds_read2_b32 v[88:89], v81 offset0:0 offset1:32
	ds_read2_b32 v[90:91], v81 offset0:64 offset1:96
	ds_read2_b32 v[92:93], v81 offset0:128 offset1:160
	ds_read2_b32 v[94:95], v81 offset0:192 offset1:224
	ds_read2_b32 v[96:97], v82 offset0:0 offset1:32
	ds_read2_b32 v[98:99], v82 offset0:64 offset1:96
	ds_read2_b32 v[100:101], v82 offset0:128 offset1:160
	ds_read2_b32 v[102:103], v82 offset0:192 offset1:224
	s_waitcnt lgkmcnt(0)
	v_max_f32_e32 v105, v88, v89
	v_max3_f32 v105, v105, v90, v91
	v_max3_f32 v105, v105, v92, v93
	v_max3_f32 v105, v105, v94, v95
	v_max3_f32 v105, v105, v96, v97
	v_max3_f32 v105, v105, v98, v99
	v_max3_f32 v105, v105, v100, v101
	v_max3_f32 v105, v105, v102, v103
	v_mov_b32_e32 v106, 0
	v_mov_b32_e32 v108, s79
	v_cmp_lt_f32_e32 vcc, 0, v105
	s_and_saveexec_b64 s[58:59], vcc
	v_div_scale_f32 v109, s[10:11], v105, v105, v108
	v_rcp_f32_e32 v110, v109
	s_nop 0
	v_fma_f32 v111, -v109, v110, 1.0
	v_fmac_f32_e32 v110, v111, v110
	v_div_scale_f32 v111, vcc, v108, v105, v108
	v_mul_f32_e32 v112, v111, v110
	v_fma_f32 v84, -v109, v112, v111
	v_fmac_f32_e32 v112, v84, v110
	v_fma_f32 v109, -v109, v112, v111
	v_div_fmas_f32 v109, v109, v110, v112
	v_div_fixup_f32 v106, v109, v105, v108
	s_mov_b64 exec, s[58:59]
	s_nop 0
	v_pk_mul_f32 v[4:5], v[106:107], v[4:5] op_sel_hi:[0,1]
	v_pk_mul_f32 v[6:7], v[106:107], v[6:7] op_sel_hi:[0,1]
	v_pk_mul_f32 v[8:9], v[106:107], v[8:9] op_sel_hi:[0,1]
	v_pk_mul_f32 v[10:11], v[106:107], v[10:11] op_sel_hi:[0,1]
	v_pk_mul_f32 v[12:13], v[106:107], v[12:13] op_sel_hi:[0,1]
	v_pk_mul_f32 v[14:15], v[106:107], v[14:15] op_sel_hi:[0,1]
	v_pk_mul_f32 v[16:17], v[106:107], v[16:17] op_sel_hi:[0,1]
	v_pk_mul_f32 v[18:19], v[106:107], v[18:19] op_sel_hi:[0,1]
	v_pk_mul_f32 v[20:21], v[106:107], v[20:21] op_sel_hi:[0,1]
	v_pk_mul_f32 v[22:23], v[106:107], v[22:23] op_sel_hi:[0,1]
	v_pk_mul_f32 v[24:25], v[106:107], v[24:25] op_sel_hi:[0,1]
	v_pk_mul_f32 v[26:27], v[106:107], v[26:27] op_sel_hi:[0,1]
	v_pk_mul_f32 v[28:29], v[106:107], v[28:29] op_sel_hi:[0,1]
	v_pk_mul_f32 v[30:31], v[106:107], v[30:31] op_sel_hi:[0,1]
	v_pk_mul_f32 v[32:33], v[106:107], v[32:33] op_sel_hi:[0,1]
	v_pk_mul_f32 v[34:35], v[106:107], v[34:35] op_sel_hi:[0,1]
	v_pk_mul_f32 v[36:37], v[106:107], v[36:37] op_sel_hi:[0,1]
	v_pk_mul_f32 v[38:39], v[106:107], v[38:39] op_sel_hi:[0,1]
	v_pk_mul_f32 v[40:41], v[106:107], v[40:41] op_sel_hi:[0,1]
	v_pk_mul_f32 v[42:43], v[106:107], v[42:43] op_sel_hi:[0,1]
	v_pk_mul_f32 v[44:45], v[106:107], v[44:45] op_sel_hi:[0,1]
	v_pk_mul_f32 v[46:47], v[106:107], v[46:47] op_sel_hi:[0,1]
	v_pk_mul_f32 v[48:49], v[106:107], v[48:49] op_sel_hi:[0,1]
	v_pk_mul_f32 v[50:51], v[106:107], v[50:51] op_sel_hi:[0,1]
	v_pk_mul_f32 v[52:53], v[106:107], v[52:53] op_sel_hi:[0,1]
	v_pk_mul_f32 v[54:55], v[106:107], v[54:55] op_sel_hi:[0,1]
	v_pk_mul_f32 v[56:57], v[106:107], v[56:57] op_sel_hi:[0,1]
	v_pk_mul_f32 v[62:63], v[106:107], v[62:63] op_sel_hi:[0,1]
	v_pk_mul_f32 v[64:65], v[106:107], v[64:65] op_sel_hi:[0,1]
	v_pk_mul_f32 v[66:67], v[106:107], v[66:67] op_sel_hi:[0,1]
	v_pk_mul_f32 v[68:69], v[106:107], v[68:69] op_sel_hi:[0,1]
	v_pk_mul_f32 v[70:71], v[106:107], v[70:71] op_sel_hi:[0,1]
	s_cmp_eq_u32 s78, 1
	s_cbranch_scc1 .Lp0h_fp8_A
; #define GAS __attribute__((address_space(1)))
; __device__ __forceinline__ void lds_barrier() { asm volatile("s_waitcnt lgkmcnt(0)" ::: "memory"); __builtin_amdgcn_s_barrier(); asm volatile("" ::: "memory"); }
; __device__ __forceinline__ void p0_panels(Frame& F) {
;     ...
;         if (okc) {
;             if (ks == 0) cur.cmax[nd] = __float_as_uint(cm);
;             GAS v4u* dst = (GAS v4u*)(cur.WT + (size_t)nd * 1024 + 64 * ks);
; #pragma unroll 1
;             for (int g4 = 0; g4 < 4; ++g4) { unsigned w[4];
; #pragma unroll
;             for (int gg = 0; gg < 4; ++gg) { const int g = 4 * g4 + gg; const int kb = (64 * ks + 4 * g) * 32 + n;
;                 const float x0 = pan[kb] * inv, x1 = pan[kb + 32] * inv, x2 = pan[kb + 64] * inv, x3 = pan[kb + 96] * inv;
;                 if (cur.fp8) { int v = __builtin_amdgcn_cvt_pk_fp8_f32(x0, x1, 0, false); v = __builtin_amdgcn_cvt_pk_fp8_f32(x2, x3, v, true); w[gg] = (unsigned)v; }
;                 else w[gg] = pack_i8x4(x0, x1, x2, x3); }
;             dst[g4] = (v4u){w[0], w[1], w[2], w[3]}; } }
;         lds_barrier();
;         if (!more) break;
	v_pk_add_f32 v[4:5], v[4:5], s[86:87] op_sel_hi:[1,0]
	v_pk_add_f32 v[6:7], v[6:7], s[86:87] op_sel_hi:[1,0]
	v_pk_add_f32 v[8:9], v[8:9], s[86:87] op_sel_hi:[1,0]
	v_pk_add_f32 v[10:11], v[10:11], s[86:87] op_sel_hi:[1,0]
	v_pk_add_f32 v[12:13], v[12:13], s[86:87] op_sel_hi:[1,0]
	v_pk_add_f32 v[14:15], v[14:15], s[86:87] op_sel_hi:[1,0]
	v_pk_add_f32 v[16:17], v[16:17], s[86:87] op_sel_hi:[1,0]
	v_pk_add_f32 v[18:19], v[18:19], s[86:87] op_sel_hi:[1,0]
	v_pk_add_f32 v[20:21], v[20:21], s[86:87] op_sel_hi:[1,0]
	v_pk_add_f32 v[22:23], v[22:23], s[86:87] op_sel_hi:[1,0]
	v_pk_add_f32 v[24:25], v[24:25], s[86:87] op_sel_hi:[1,0]
	v_pk_add_f32 v[26:27], v[26:27], s[86:87] op_sel_hi:[1,0]
	v_pk_add_f32 v[28:29], v[28:29], s[86:87] op_sel_hi:[1,0]
	v_pk_add_f32 v[30:31], v[30:31], s[86:87] op_sel_hi:[1,0]
	v_pk_add_f32 v[32:33], v[32:33], s[86:87] op_sel_hi:[1,0]
	v_pk_add_f32 v[34:35], v[34:35], s[86:87] op_sel_hi:[1,0]
	v_pk_add_f32 v[36:37], v[36:37], s[86:87] op_sel_hi:[1,0]
	v_pk_add_f32 v[38:39], v[38:39], s[86:87] op_sel_hi:[1,0]
	v_pk_add_f32 v[40:41], v[40:41], s[86:87] op_sel_hi:[1,0]
	v_pk_add_f32 v[42:43], v[42:43], s[86:87] op_sel_hi:[1,0]
	v_pk_add_f32 v[44:45], v[44:45], s[86:87] op_sel_hi:[1,0]
	v_pk_add_f32 v[46:47], v[46:47], s[86:87] op_sel_hi:[1,0]
	v_pk_add_f32 v[48:49], v[48:49], s[86:87] op_sel_hi:[1,0]
	v_pk_add_f32 v[50:51], v[50:51], s[86:87] op_sel_hi:[1,0]
	v_pk_add_f32 v[52:53], v[52:53], s[86:87] op_sel_hi:[1,0]
	v_pk_add_f32 v[54:55], v[54:55], s[86:87] op_sel_hi:[1,0]
	v_pk_add_f32 v[56:57], v[56:57], s[86:87] op_sel_hi:[1,0]
	v_pk_add_f32 v[62:63], v[62:63], s[86:87] op_sel_hi:[1,0]
	v_pk_add_f32 v[64:65], v[64:65], s[86:87] op_sel_hi:[1,0]
	v_pk_add_f32 v[66:67], v[66:67], s[86:87] op_sel_hi:[1,0]
	v_pk_add_f32 v[68:69], v[68:69], s[86:87] op_sel_hi:[1,0]
	v_pk_add_f32 v[70:71], v[70:71], s[86:87] op_sel_hi:[1,0]
	v_perm_b32 v85, v5, v4, s88
	v_perm_b32 v86, v7, v6, s89
	v_or_b32_e32 v88, v85, v86
	v_perm_b32 v85, v9, v8, s88
	v_perm_b32 v86, v11, v10, s89
	v_or_b32_e32 v89, v85, v86
	v_perm_b32 v85, v13, v12, s88
	v_perm_b32 v86, v15, v14, s89
	v_or_b32_e32 v90, v85, v86
	v_perm_b32 v85, v17, v16, s88
	v_perm_b32 v86, v19, v18, s89
	v_or_b32_e32 v91, v85, v86
	v_perm_b32 v85, v21, v20, s88
	v_perm_b32 v86, v23, v22, s89
	v_or_b32_e32 v92, v85, v86
	v_perm_b32 v85, v25, v24, s88
	v_perm_b32 v86, v27, v26, s89
	v_or_b32_e32 v93, v85, v86
	v_perm_b32 v85, v29, v28, s88
	v_perm_b32 v86, v31, v30, s89
	v_or_b32_e32 v94, v85, v86
	v_perm_b32 v85, v33, v32, s88
	v_perm_b32 v86, v35, v34, s89
	v_or_b32_e32 v95, v85, v86
	v_perm_b32 v85, v37, v36, s88
	v_perm_b32 v86, v39, v38, s89
	v_or_b32_e32 v96, v85, v86
	v_perm_b32 v85, v41, v40, s88
	v_perm_b32 v86, v43, v42, s89
	v_or_b32_e32 v97, v85, v86
	v_perm_b32 v85, v45, v44, s88
	v_perm_b32 v86, v47, v46, s89
	v_or_b32_e32 v98, v85, v86
	v_perm_b32 v85, v49, v48, s88
	v_perm_b32 v86, v51, v50, s89
	v_or_b32_e32 v99, v85, v86
	v_perm_b32 v85, v53, v52, s88
	v_perm_b32 v86, v55, v54, s89
	v_or_b32_e32 v100, v85, v86
	v_perm_b32 v85, v57, v56, s88
	v_perm_b32 v86, v63, v62, s89
	v_or_b32_e32 v101, v85, v86
	v_perm_b32 v85, v65, v64, s88
	v_perm_b32 v86, v67, v66, s89
	v_or_b32_e32 v102, v85, v86
	v_perm_b32 v85, v69, v68, s88
	v_perm_b32 v86, v71, v70, s89
	v_or_b32_e32 v103, v85, v86
	s_branch .Lp0h_st_A
.Lp0h_fp8_A:
	v_cvt_pk_fp8_f32 v88, v4, v5
	v_cvt_pk_fp8_f32 v88, v6, v7 op_sel:[0,0,1]
	v_cvt_pk_fp8_f32 v89, v8, v9
	v_cvt_pk_fp8_f32 v89, v10, v11 op_sel:[0,0,1]
	v_cvt_pk_fp8_f32 v90, v12, v13
	v_cvt_pk_fp8_f32 v90, v14, v15 op_sel:[0,0,1]
	v_cvt_pk_fp8_f32 v91, v16, v17
	v_cvt_pk_fp8_f32 v91, v18, v19 op_sel:[0,0,1]
	v_cvt_pk_fp8_f32 v92, v20, v21
	v_cvt_pk_fp8_f32 v92, v22, v23 op_sel:[0,0,1]
	v_cvt_pk_fp8_f32 v93, v24, v25
	v_cvt_pk_fp8_f32 v93, v26, v27 op_sel:[0,0,1]
	v_cvt_pk_fp8_f32 v94, v28, v29
	v_cvt_pk_fp8_f32 v94, v30, v31 op_sel:[0,0,1]
	v_cvt_pk_fp8_f32 v95, v32, v33
	v_cvt_pk_fp8_f32 v95, v34, v35 op_sel:[0,0,1]
	v_cvt_pk_fp8_f32 v96, v36, v37
	v_cvt_pk_fp8_f32 v96, v38, v39 op_sel:[0,0,1]
	v_cvt_pk_fp8_f32 v97, v40, v41
	v_cvt_pk_fp8_f32 v97, v42, v43 op_sel:[0,0,1]
	v_cvt_pk_fp8_f32 v98, v44, v45
	v_cvt_pk_fp8_f32 v98, v46, v47 op_sel:[0,0,1]
	v_cvt_pk_fp8_f32 v99, v48, v49
	v_cvt_pk_fp8_f32 v99, v50, v51 op_sel:[0,0,1]
	v_cvt_pk_fp8_f32 v100, v52, v53
	v_cvt_pk_fp8_f32 v100, v54, v55 op_sel:[0,0,1]
	v_cvt_pk_fp8_f32 v101, v56, v57
	v_cvt_pk_fp8_f32 v101, v62, v63 op_sel:[0,0,1]
	v_cvt_pk_fp8_f32 v102, v64, v65
	v_cvt_pk_fp8_f32 v102, v66, v67 op_sel:[0,0,1]
	v_cvt_pk_fp8_f32 v103, v68, v69
	v_cvt_pk_fp8_f32 v103, v70, v71 op_sel:[0,0,1]
.Lp0h_st_A:
	s_mov_b64 exec, s[76:77]
	global_store_dwordx4 v83, v[88:91], s[72:73]
	global_store_dwordx4 v83, v[92:95], s[72:73] offset:16
	global_store_dwordx4 v83, v[96:99], s[72:73] offset:32
	global_store_dwordx4 v83, v[100:103], s[72:73] offset:48
	s_and_b64 exec, exec, s[56:57]
	global_store_dword v80, v105, s[74:75]
	s_mov_b64 exec, -1
	s_barrier
	s_cmp_eq_u32 s83, 0
	s_cbranch_scc1 .Lp0h_nob1
	ds_write_b128 v74, v[114:117]
	ds_write_b128 v74, v[118:121] offset:8192
	ds_write_b128 v74, v[122:125] offset:16384
	ds_write_b128 v74, v[126:129] offset:24576
	ds_write_b128 v74, v[130:133] offset:32768
	ds_write_b128 v74, v[134:137] offset:40960
	ds_write_b128 v74, v[138:141] offset:49152
	ds_write_b128 v74, v[142:145] offset:57344
	ds_write_b128 v75, v[146:149]
	ds_write_b128 v75, v[150:153] offset:8192
	ds_write_b128 v75, v[154:157] offset:16384
	ds_write_b128 v75, v[158:161] offset:24576
	ds_write_b128 v75, v[162:165] offset:32768
	ds_write_b128 v75, v[166:169] offset:40960
	ds_write_b128 v75, v[170:173] offset:49152
	ds_write_b128 v75, v[174:177] offset:57344
	s_waitcnt lgkmcnt(0)
	s_barrier
.Lp0h_nob1:
	s_add_i32 s84, s84, s94
	s_cmpk_lt_i32 s84, 0xc6a
	s_cbranch_scc0 .Lp0h_nonext
	s_cmpk_lt_i32 s84, 0x635
	s_cselect_b32 s65, 0, 0x635
	s_cselect_b32 s66, 0, 0xc71
	s_sub_i32 s67, s84, s65
	s_mov_b32 s9, 1
	s_cmpk_lt_i32 s67, 53
	s_cbranch_scc0 .Lp0h_cv_gu_c1
	s_lshl_b32 s68, s67, 1
	s_cmpk_eq_i32 s67, 52
	s_cselect_b32 s9, 0, 1
	s_branch .Lp0h_cv_done_c1

; __device__ __forceinline__ const GAS float* inp(const Frame& F, int i) { return (const GAS float*)*(const float* const __attribute__((address_space(4)))*)(F.ka + 8 * i); }
; __device__ __forceinline__ bf16* w_in_t(Frame& F, int l)  { return (bf16*)(F.ws + WS_W + (size_t)l * W_LAYER_B); }
; __device__ __forceinline__ bf16* w_gu_t(Frame& F, int l)  { return (bf16*)(F.ws + WS_W + (size_t)l * W_LAYER_B + W_IN_B + W_OUT_B); }
; __device__ __forceinline__ bf16* w_dn_t(Frame& F, int l)  { return (bf16*)(F.ws + WS_W + (size_t)l * W_LAYER_B + W_IN_B + W_OUT_B + W_GU_B); }
; __device__ __forceinline__ PanelSrc p0_panel_src(Frame& F, int it) {
;     constexpr int P_IN = (NPROJ + 31) / 32 + 8, P_GU = 2048 / 32, P_DN = D / 32, PAN_LAYER = P_IN + NEXP * P_GU + NEXP * P_DN;
;     const int l = it / PAN_LAYER; int r = it % PAN_LAYER; PanelSrc s; s.W2 = inp(F, 4) + (size_t)l * GLR_RANK * 256;
;     if (r < P_IN) { s.W = inp(F, 3) + (size_t)l * D * NPROJ; s.N = NPROJ; s.WT = (signed char*)w_in_t(F, l); s.cmax = F.ctl + CW_CMAX_IN + l * NPROJ_PAD; s.fp8 = 0;
;         if (r < P_IN - 8) { s.p = r; s.mode = 2; } else { s.p = r - (P_IN - 8); s.mode = 3; } }
;     else if (r < P_IN + NEXP * P_GU) { r -= P_IN; const int e = r / P_GU; s.W = inp(F, 15) + ((size_t)l * NEXP + e) * D * 2048; s.N = 2048; s.WT = (signed char*)w_gu_t(F, l) + (size_t)e * 2048 * D; s.cmax = F.ctl + CW_CMAX_GU + (l * NEXP + e) * 2048; s.p = r % P_GU; s.mode = 1; s.fp8 = 0; }
;     else { r -= P_IN + NEXP * P_GU; const int e = r / P_DN; s.W = inp(F, 17) + ((size_t)l * NEXP + e) * DFF * D; s.N = D; s.WT = (signed char*)w_dn_t(F, l) + (size_t)e * D * DFF; s.cmax = F.ctl + CW_CMAX_DN + (l * NEXP + e) * D; s.p = r % P_DN; s.mode = 0; s.fp8 = 1; }
.Lp0h_cv_done_c1:
	s_add_i32 s82, s68, s66
	s_cmpk_lt_i32 s82, 0xc71
	s_cselect_b32 s65, 0, 0xc71
	s_cselect_b32 s66, 0, 1
	s_sub_i32 s67, s82, s65
	s_mov_b32 s64, 0
	s_cmpk_lt_i32 s67, 0x71
	s_cbranch_scc0 .Lp0h_dl_gu_p1
	s_mul_i32 s68, s66, 0xd10000
	s_lshl_b32 s69, s67, 7
	s_add_u32 s68, s68, s69
	s_add_u32 s60, s50, s68
	s_addc_u32 s61, s51, 0
	s_movk_i32 s62, 0x3440
	s_mov_b32 s63, 0xd1000
	s_cmpk_eq_i32 s67, 0x68
	s_cselect_b32 s64, 1, 0
	s_branch .Lp0h_dl_done_p1

; __device__ __forceinline__ void p0_panels(Frame& F) {
;     ...
;         const int ns = 32 * cur.p + n; int nd = ns; bool okc = ns < cur.N;
;         if (cur.mode == 1) { const int half = ns >> 10, cc = ns & 1023; nd = (cc >> 7) * 256 + half * 128 + (cc & 127); }
;         else if (cur.mode == 2) { nd = ns < SRC_GLR ? ns : ns + (C_GOG - SRC_GLR - GLR_RANK); okc = okc && !(ns >= SRC_GLR && ns < SRC_GLR + GLR_RANK); }
;         else if (cur.mode == 3) { nd = C_GLG + ns; okc = ns < 256; }
.Lp0h_ldone_p1:
.Lp0h_nonext:
	s_cmp_eq_u32 s83, 0
	s_cbranch_scc1 .Lp0h_nob2
	s_add_i32 s81, s80, 1
	s_cmpk_lt_i32 s81, 0xc71
	s_cselect_b32 s65, 0, 0xc71
	s_cselect_b32 s66, 0, 1
	s_sub_i32 s67, s81, s65
	s_mul_i32 s70, s66, 0xc900000
	s_mov_b64 s[76:77], -1
	s_mov_b32 s79, 0x42fe0000
	s_cmpk_lt_i32 s67, 0x71
	s_cbranch_scc0 .Lp0h_dp_gu_B
	s_lshl_b32 s71, s67, 5
	s_cmpk_lt_i32 s67, 32
	s_cselect_b32 s68, 0, 0xf0
	s_add_i32 s71, s71, s68
	s_add_u32 s70, s70, 0x200000
	s_mul_i32 s69, s66, 0x3800
	s_add_u32 s69, s69, 0x40000
	s_mov_b32 s78, 0
	s_cmpk_eq_i32 s67, 32
	s_cbranch_scc0 .Lp0h_dp_m2a_B
	s_mov_b32 s76, 0xffff0000
	s_mov_b32 s77, 0xffff0000

; __device__ __forceinline__ const GAS float* inp(const Frame& F, int i) { return (const GAS float*)*(const float* const __attribute__((address_space(4)))*)(F.ka + 8 * i); }
; __device__ __forceinline__ bf16* w_in_t(Frame& F, int l)  { return (bf16*)(F.ws + WS_W + (size_t)l * W_LAYER_B); }
; __device__ __forceinline__ bf16* w_gu_t(Frame& F, int l)  { return (bf16*)(F.ws + WS_W + (size_t)l * W_LAYER_B + W_IN_B + W_OUT_B); }
; __device__ __forceinline__ bf16* w_dn_t(Frame& F, int l)  { return (bf16*)(F.ws + WS_W + (size_t)l * W_LAYER_B + W_IN_B + W_OUT_B + W_GU_B); }
; __device__ __forceinline__ PanelSrc p0_panel_src(Frame& F, int it) {
;     constexpr int P_IN = (NPROJ + 31) / 32 + 8, P_GU = 2048 / 32, P_DN = D / 32, PAN_LAYER = P_IN + NEXP * P_GU + NEXP * P_DN;
;     const int l = it / PAN_LAYER; int r = it % PAN_LAYER; PanelSrc s; s.W2 = inp(F, 4) + (size_t)l * GLR_RANK * 256;
;     if (r < P_IN) { s.W = inp(F, 3) + (size_t)l * D * NPROJ; s.N = NPROJ; s.WT = (signed char*)w_in_t(F, l); s.cmax = F.ctl + CW_CMAX_IN + l * NPROJ_PAD; s.fp8 = 0;
;         if (r < P_IN - 8) { s.p = r; s.mode = 2; } else { s.p = r - (P_IN - 8); s.mode = 3; } }
;     else if (r < P_IN + NEXP * P_GU) { r -= P_IN; const int e = r / P_GU; s.W = inp(F, 15) + ((size_t)l * NEXP + e) * D * 2048; s.N = 2048; s.WT = (signed char*)w_gu_t(F, l) + (size_t)e * 2048 * D; s.cmax = F.ctl + CW_CMAX_GU + (l * NEXP + e) * 2048; s.p = r % P_GU; s.mode = 1; s.fp8 = 0; }
;     else { r -= P_IN + NEXP * P_GU; const int e = r / P_DN; s.W = inp(F, 17) + ((size_t)l * NEXP + e) * DFF * D; s.N = D; s.WT = (signed char*)w_dn_t(F, l) + (size_t)e * D * DFF; s.cmax = F.ctl + CW_CMAX_DN + (l * NEXP + e) * D; s.p = r % P_DN; s.mode = 0; s.fp8 = 1; }
; __device__ __forceinline__ void p0_panels(Frame& F) {
;     ...
;     int it = F.vcu; if (it >= NPAN) return;
;     float rg[64]; PanelSrc cur = p0_panel_src(F, it); p0_panel_load(F, cur, rg);
;     for (;;) {
; #pragma unroll
;         for (int i = 0; i < 64; ++i) { const int k = 2 * (8 * i + wave) + (lane >> 5); pan[k * 32 + (lane & 31)] = rg[i]; }
;         lds_barrier();
;         const int itn = it + F.G; const bool more = itn < NPAN; PanelSrc nxt = cur; if (more) { nxt = p0_panel_src(F, itn); p0_panel_load(F, nxt, rg); }
.Lp0h_st_B:
	s_mov_b64 exec, s[76:77]
	global_store_dwordx4 v83, v[88:91], s[72:73]
	global_store_dwordx4 v83, v[92:95], s[72:73] offset:16
	global_store_dwordx4 v83, v[96:99], s[72:73] offset:32
	global_store_dwordx4 v83, v[100:103], s[72:73] offset:48
	s_and_b64 exec, exec, s[56:57]
	global_store_dword v80, v105, s[74:75]
	s_mov_b64 exec, -1
	s_barrier
.Lp0h_nob2:
	s_mov_b32 s80, s82
	s_mov_b32 s83, s9
	s_cmpk_lt_i32 s84, 0xc6a
	s_cbranch_scc1 .Lp0h_top
.Lp0h_done:
	s_sub_i32 s65, s8, 0xea
	s_cmp_lt_u32 s65, 16
	s_cbranch_scc0 .LBB0_255
	s_add_i32 s8, s65, 0x69
	s_cmp_lt_u32 s65, 8
	s_cbranch_scc1 .Lp0h_m3
	s_add_i32 s8, s65, 0xcd2
.Lp0h_m3:
	s_movk_i32 s99, 0x4000
.Lp0h_orig:
	s_mul_hi_i32 s0, s8, 0x524e4977
	s_lshr_b32 s1, s0, 31
	s_ashr_i32 s0, s0, 10
	s_add_i32 s4, s0, s1
	s_mul_i32 s0, s4, 0xc71
	s_sub_i32 s3, s8, s0
	s_ashr_i32 s5, s4, 31
	s_mul_hi_i32 s2, s4, 0xc900000
	s_cmpk_gt_i32 s3, 0x70
	s_mul_i32 s10, s4, 0xc900000
	v_writelane_b32 v252, s30, 7
	s_cbranch_scc0 .LBB0_12
	v_mov_b32_e32 v0, 0x871
	v_sub_co_u32_e32 v0, vcc, s3, v0
	s_add_u32 s0, s42, s10
	s_addc_u32 s1, s43, s2
	s_andn2_b64 vcc, exec, vcc
	s_mov_b32 s9, 1
	s_cbranch_vccz .LBB0_301
	s_load_dwordx2 s[12:13], s[40:41], 0x88
	s_lshl_b64 s[6:7], s[4:5], 27
	s_lshl_b32 s8, s4, 15
	v_lshrrev_b32_e32 v2, 5, v0
	v_mov_b32_e32 v3, 0
	s_waitcnt lgkmcnt(0)
	s_add_u32 s6, s12, s6
	v_lshlrev_b64 v[4:5], 22, v[2:3]
	v_lshlrev_b64 v[6:7], 20, v[2:3]
	v_lshlrev_b32_e32 v1, 10, v2
	s_addc_u32 s7, s13, s7
	v_add_u32_e32 v102, s8, v1
	v_and_b32_e32 v115, 31, v0
	v_lshl_add_u64 v[110:111], s[6:7], 0, v[4:5]
	v_lshl_add_u64 v[0:1], s[0:1], 0, v[6:7]
	s_mov_b64 s[6:7], 0x8b00000
	v_lshl_add_u64 v[56:57], v[0:1], 0, s[6:7]
	s_cbranch_execz .LBB0_302
	s_mov_b64 s[14:15], 0x100000
	s_movk_i32 s88, 0x400
	s_mov_b32 s33, 0
	s_cbranch_execz .LBB0_13
	s_branch .LBB0_14

; __device__ __forceinline__ void lds_barrier() { asm volatile("s_waitcnt lgkmcnt(0)" ::: "memory"); __builtin_amdgcn_s_barrier(); asm volatile("" ::: "memory"); }
; __device__ __forceinline__ void p0_panels(Frame& F) {
;     ...
;     for (;;) {
; #pragma unroll
;         for (int i = 0; i < 64; ++i) { const int k = 2 * (8 * i + wave) + (lane >> 5); pan[k * 32 + (lane & 31)] = rg[i]; }
;         lds_barrier();
;         const int itn = it + F.G; const bool more = itn < NPAN; PanelSrc nxt = cur; if (more) { nxt = p0_panel_src(F, itn); p0_panel_load(F, nxt, rg); }
.LBB0_87:
	s_add_i32 s13, s2, s94
	s_add_i32 s13, s13, s99
	s_waitcnt vmcnt(0)
	ds_write2st64_b32 v27, v63, v62 offset1:8
	ds_write2st64_b32 v27, v65, v64 offset0:16 offset1:24
	ds_write2st64_b32 v27, v67, v66 offset0:32 offset1:40
	ds_write2st64_b32 v27, v69, v68 offset0:48 offset1:56
	ds_write2st64_b32 v27, v71, v70 offset0:64 offset1:72
	ds_write2st64_b32 v27, v73, v72 offset0:80 offset1:88
	ds_write2st64_b32 v27, v75, v74 offset0:96 offset1:104
	ds_write2st64_b32 v27, v77, v76 offset0:112 offset1:120
	ds_write2st64_b32 v27, v79, v78 offset0:128 offset1:136
	ds_write2st64_b32 v27, v81, v80 offset0:144 offset1:152
	ds_write2st64_b32 v27, v83, v82 offset0:160 offset1:168
	ds_write2st64_b32 v27, v85, v84 offset0:176 offset1:184
	ds_write2st64_b32 v27, v87, v86 offset0:192 offset1:200
	ds_write2st64_b32 v27, v89, v88 offset0:208 offset1:216
	ds_write2st64_b32 v27, v91, v90 offset0:224 offset1:232
	ds_write2st64_b32 v27, v93, v92 offset0:240 offset1:248
	ds_write_b32 v35, v99
	ds_write_b32 v37, v98
	ds_write_b32 v39, v105
	ds_write_b32 v41, v104
	ds_write_b32 v43, v107
	ds_write_b32 v45, v106
	ds_write_b32 v47, v109
	ds_write_b32 v49, v108
	ds_write_b32 v51, v201
	ds_write_b32 v53, v200
	ds_write_b32 v55, v203
	ds_write_b32 v101, v202
	ds_write_b32 v103, v205
	ds_write_b32 v111, v204
	ds_write_b32 v117, v207
	ds_write_b32 v119, v206
	ds_write_b32 v121, v209
	ds_write_b32 v123, v208
	ds_write_b32 v125, v211
	ds_write_b32 v127, v210
	ds_write_b32 v129, v213
	ds_write_b32 v131, v212
	ds_write_b32 v133, v215
	ds_write_b32 v135, v214
	ds_write_b32 v137, v217
	ds_write_b32 v139, v216
	ds_write_b32 v141, v251
	ds_write_b32 v143, v250
	ds_write_b32 v145, v221
	ds_write_b32 v147, v220
	ds_write_b32 v149, v5
	ds_write_b32 v151, v4
	s_cmpk_lt_i32 s13, 0x18e2
	s_waitcnt lgkmcnt(0)
	s_barrier
	s_cselect_b64 s[18:19], -1, 0
	s_cmpk_gt_i32 s13, 0x18e1
	s_cselect_b64 s[16:17], -1, 0
	s_and_b64 vcc, exec, s[16:17]
	s_mov_b32 s6, s88
	v_mov_b64_e32 v[6:7], v[56:57]
	v_mov_b64_e32 v[8:9], v[20:21]
	v_mov_b32_e32 v159, v115
	s_mov_b32 s87, s33
	s_mov_b32 s3, s9
	s_cbranch_vccnz .LBB0_164
	s_mul_hi_i32 s3, s13, 0x524e4977
	s_lshr_b32 s4, s3, 31
	s_ashr_i32 s3, s3, 10
	s_add_i32 s4, s3, s4
	s_mul_i32 s3, s4, 0xc71
	s_sub_i32 s26, s13, s3
	s_ashr_i32 s5, s4, 31
	s_mov_b64 s[22:23], -1
	s_cmpk_gt_i32 s26, 0x70
	s_mul_hi_i32 s27, s4, 0xc900000
	s_mul_i32 s29, s4, 0xc900000
	s_cbranch_scc0 .LBB0_93
	s_add_u32 s30, s42, s29
	s_addc_u32 s31, s43, s27
	s_cmpk_gt_u32 s26, 0x870
	s_cbranch_scc0 .LBB0_91
	s_load_dwordx2 s[10:11], s[40:41], 0x88
	s_add_i32 s3, s26, 0xfffff78f
	s_lshl_b64 s[20:21], s[4:5], 27
	s_lshr_b32 s6, s3, 5
	s_mov_b64 s[22:23], 0
	s_waitcnt lgkmcnt(0)
	s_add_u32 s20, s10, s20
	s_addc_u32 s21, s11, s21
	s_lshl_b64 s[10:11], s[6:7], 22
	s_add_u32 s24, s20, s10
	s_addc_u32 s25, s21, s11
	s_lshl_b64 s[10:11], s[6:7], 20
	s_add_u32 s10, s30, s10
	s_addc_u32 s11, s31, s11
	s_add_u32 s20, s10, 0x8b00000
	s_addc_u32 s21, s11, 0
	s_lshl_b32 s10, s4, 15
	s_lshl_b32 s6, s6, 10
	s_add_i32 s10, s6, s10
	s_ashr_i32 s11, s10, 31
	s_lshl_b64 s[10:11], s[10:11], 2
	v_readlane_b32 s6, v252, 13
	s_add_u32 s10, s6, s10
	v_readlane_b32 s6, v252, 14
	s_addc_u32 s11, s6, s11
	s_and_b32 s28, s3, 31
